# attention: all 7 ring DMA pieces issued in the first four P.V MFMA gaps (land while LDS is idle), row-max under P.V (on v11)
# baseline (speedup 1.0000x reference)
.LBB0_1235:
	s_add_i32 s15, s14, 1
	s_cmp_lg_u32 s14, 2
	s_cselect_b32 s14, s15, 0
	s_mul_i32 s15, s14, 0x6400
	v_add_u32_e32 v70, s15, v185
	ds_read_b128 v[66:69], v70
	ds_read_b128 v[166:169], v70 offset:32
	ds_read_b128 v[170:173], v70 offset:64
	ds_read_b128 v[188:191], v70 offset:96
	ds_read_b128 v[192:195], v70 offset:128
	ds_read_b128 v[196:199], v70 offset:160
	ds_read_b128 v[200:203], v70 offset:192
	ds_read_b128 v[216:219], v70 offset:224
	ds_read_b128 v[220:223], v70 offset:256
	ds_read_b128 v[224:227], v70 offset:288
	ds_read_b128 v[228:231], v70 offset:320
	ds_read_b128 v[146:149], v70 offset:352
	s_waitcnt lgkmcnt(11)
	v_mfma_f32_32x32x16_bf16 v[66:81], v[66:69], v[142:145], 0
	v_sub_f32_e32 v82, v82, v183
	v_exp_f32_e32 v82, v82
	v_sub_f32_e32 v94, v94, v183
	v_exp_f32_e32 v94, v94
	v_add_f32_e32 v165, 0, v82
	v_add_f32_e32 v165, v94, v165
	s_waitcnt lgkmcnt(10)
	v_mfma_f32_32x32x16_bf16 v[66:81], v[166:169], v[138:141], v[66:81]
	v_sub_f32_e32 v83, v83, v183
	v_exp_f32_e32 v83, v83
	v_sub_f32_e32 v95, v95, v183
	v_exp_f32_e32 v95, v95
	v_add_f32_e32 v165, v83, v165
	v_cvt_pk_bf16_f32 v82, v82, v83
	v_add_f32_e32 v165, v95, v165
	v_sub_f32_e32 v83, v84, v183
	s_waitcnt lgkmcnt(9)
	v_mfma_f32_32x32x16_bf16 v[66:81], v[170:173], v[134:137], v[66:81]
	v_exp_f32_e32 v83, v83
	v_sub_f32_e32 v96, v96, v183
	v_add_f32_e32 v84, v83, v165
	v_exp_f32_e32 v165, v96
	s_nop 0
	v_add_f32_e32 v84, v165, v84
	s_waitcnt lgkmcnt(8)
	v_mfma_f32_32x32x16_bf16 v[66:81], v[188:191], v[130:133], v[66:81]
	v_sub_f32_e32 v85, v85, v183
	v_exp_f32_e32 v85, v85
	v_sub_f32_e32 v96, v97, v183
	v_exp_f32_e32 v97, v96
	v_cvt_pk_bf16_f32 v96, v94, v95
	v_add_f32_e32 v84, v85, v84
	v_cvt_pk_bf16_f32 v83, v83, v85
	v_add_f32_e32 v84, v97, v84
	v_cvt_pk_bf16_f32 v97, v165, v97
	s_waitcnt lgkmcnt(7)
	v_mfma_f32_32x32x16_bf16 v[66:81], v[192:195], v[126:129], v[66:81]
	v_sub_f32_e32 v85, v86, v183
	v_exp_f32_e32 v85, v85
	s_nop 0
	v_add_f32_e32 v84, v85, v84
	s_waitcnt lgkmcnt(6)
	v_mfma_f32_32x32x16_bf16 v[66:81], v[196:199], v[122:125], v[66:81]
	v_sub_f32_e32 v86, v87, v183
	v_exp_f32_e32 v86, v86
	s_nop 0
	v_add_f32_e32 v87, v86, v84
	v_cvt_pk_bf16_f32 v84, v85, v86
	s_waitcnt lgkmcnt(5)
	v_mfma_f32_32x32x16_bf16 v[66:81], v[200:203], v[118:121], v[66:81]
	v_sub_f32_e32 v85, v88, v183
	v_exp_f32_e32 v85, v85
	s_nop 0
	v_add_f32_e32 v86, v85, v87
	s_waitcnt lgkmcnt(4)
	v_mfma_f32_32x32x16_bf16 v[66:81], v[216:219], v[114:117], v[66:81]
	v_sub_f32_e32 v87, v89, v183
	v_exp_f32_e32 v87, v87
	s_nop 0
	v_add_f32_e32 v86, v87, v86
	v_cvt_pk_bf16_f32 v85, v85, v87
	v_sub_f32_e32 v87, v90, v183
	v_exp_f32_e32 v90, v87
	s_waitcnt lgkmcnt(3)
	v_mfma_f32_32x32x16_bf16 v[66:81], v[220:223], v[110:113], v[66:81]
	v_add_u32_e32 v165, s13, v187
	v_add_f32_e32 v94, v90, v86
	ds_read_b128 v[86:89], v165
	ds_read_b128 v[166:169], v165 offset:32
	s_waitcnt lgkmcnt(4)
	v_mfma_f32_32x32x16_bf16 v[66:81], v[224:227], v[106:109], v[66:81]
	v_sub_f32_e32 v91, v91, v183
	ds_read_b128 v[170:173], v165 offset:4608
	ds_read_b128 v[188:191], v165 offset:4640
	v_exp_f32_e32 v91, v91
	s_nop 0
	v_add_f32_e32 v95, v91, v94
	v_cvt_pk_bf16_f32 v94, v90, v91
	s_waitcnt lgkmcnt(5)
	v_mfma_f32_32x32x16_bf16 v[66:81], v[228:231], v[102:105], v[66:81]
	v_sub_f32_e32 v90, v92, v183
	ds_read_b128 v[192:195], v165 offset:9216
	ds_read_b128 v[196:199], v165 offset:9248
	v_exp_f32_e32 v90, v90
	s_nop 0
	v_add_f32_e32 v91, v90, v95
	v_sub_f32_e32 v92, v93, v183
	v_exp_f32_e32 v92, v92
	s_waitcnt lgkmcnt(6)
	v_mfma_f32_32x32x16_bf16 v[66:81], v[146:149], v[98:101], v[66:81]
	v_add_f32_e32 v186, v92, v91
	v_cvt_pk_bf16_f32 v95, v90, v92
	ds_read_b128 v[90:93], v165 offset:13824
	ds_read_b128 v[146:149], v165 offset:13856
	s_orn2_b64 vcc, s[0:1], s[24:25]
	s_and_b64 vcc, vcc, exec
	s_cbranch_vccnz .LattB_slow
	s_mul_i32 s13, s12, 0x6400
	s_add_u32 s16, s80, s2
	s_addc_u32 s17, s81, s3
	s_add_u32 s16, s16, 0x30e90000
	s_addc_u32 s17, s17, 0
	s_waitcnt lgkmcnt(0)
	v_mfma_f32_32x32x16_bf16 v[50:65], v[86:89], v[82:85], v[50:65]
	v_add_f32_e32 v186, v164, v186
	s_add_i32 m0, s13, s65
	s_nop 0
	global_load_lds_dwordx4 v208, s[16:17]
	s_add_i32 m0, s13, s66
	s_nop 0
	global_load_lds_dwordx4 v209, s[16:17]
	v_mfma_f32_32x32x16_bf16 v[34:49], v[170:173], v[82:85], v[34:49]
	s_add_i32 m0, s13, s67
	s_add_i32 s13, s13, s68
	global_load_lds_dwordx4 v210, s[16:17]
	s_add_i32 m0, s13, 0x6000
	s_nop 0
	global_load_lds_dwordx4 v211, s[16:17]
	v_mfma_f32_32x32x16_bf16 v[18:33], v[192:195], v[82:85], v[18:33]
	v_max_f32_e32 v150, v66, v67
	v_max3_f32 v150, v150, v68, v69
	s_mul_i32 s13, s12, 0x4800
	s_add_i32 s15, s13, 0xffffb800
	s_cmp_lg_u32 s12, 0
	s_cselect_b32 s15, s15, 0x9000
	s_add_i32 s15, s15, 0x12c00
	s_add_u32 s16, s82, s2
	s_addc_u32 s17, s83, s3
	s_add_u32 s16, s16, 0x31bf8180
	s_addc_u32 s17, s17, 0
	s_add_i32 m0, s15, s69
	s_nop 0
	global_load_lds_dwordx4 v212, s[16:17]
	v_mfma_f32_32x32x16_bf16 v[2:17], v[90:93], v[82:85], v[2:17]
	v_max3_f32 v150, v150, v70, v71
	v_max3_f32 v150, v150, v72, v73
	s_add_i32 m0, s15, s70
	s_nop 0
	global_load_lds_dwordx4 v213, s[16:17]
	s_add_i32 m0, s15, s71
	s_nop 0
	global_load_lds_dwordx4 v214, s[16:17]
	v_mfma_f32_32x32x16_bf16 v[50:65], v[166:169], v[94:97], v[50:65]
	v_max3_f32 v150, v150, v74, v75
	v_max3_f32 v150, v150, v76, v77
	v_mfma_f32_32x32x16_bf16 v[34:49], v[188:191], v[94:97], v[34:49]
	v_max3_f32 v150, v150, v78, v79
	v_max3_f32 v150, v150, v80, v81
	v_mfma_f32_32x32x16_bf16 v[18:33], v[196:199], v[94:97], v[18:33]
	v_mfma_f32_32x32x16_bf16 v[2:17], v[146:149], v[94:97], v[2:17]
	v_mov_b32_e32 v151, v150
	s_nop 1
	v_permlane32_swap_b32_e32 v151, v150
	v_max_f32_e32 v150, v150, v151
	s_branch .LattB_join

.LBB0_1240:
	s_mul_i32 s13, s14, 0x6400
	v_add_u32_e32 v86, s13, v185
	ds_read_b128 v[82:85], v86
	ds_read_b128 v[188:191], v86 offset:32
	ds_read_b128 v[192:195], v86 offset:64
	ds_read_b128 v[196:199], v86 offset:96
	ds_read_b128 v[200:203], v86 offset:128
	ds_read_b128 v[216:219], v86 offset:160
	ds_read_b128 v[220:223], v86 offset:192
	ds_read_b128 v[224:227], v86 offset:224
	ds_read_b128 v[228:231], v86 offset:256
	ds_read_b128 v[232:235], v86 offset:288
	ds_read_b128 v[236:239], v86 offset:320
	ds_read_b128 v[240:243], v86 offset:352
	s_waitcnt lgkmcnt(11)
	v_mfma_f32_32x32x16_bf16 v[82:97], v[82:85], v[142:145], 0
	v_sub_f32_e32 v66, v66, v183
	v_sub_f32_e32 v78, v78, v183
	v_exp_f32_e32 v66, v66
	v_exp_f32_e32 v78, v78
	s_waitcnt lgkmcnt(10)
	v_mfma_f32_32x32x16_bf16 v[82:97], v[188:191], v[138:141], v[82:97]
	v_sub_f32_e32 v67, v67, v183
	v_sub_f32_e32 v79, v79, v183
	v_exp_f32_e32 v67, v67
	v_exp_f32_e32 v79, v79
	v_cvt_pk_bf16_f32 v188, v66, v67
	s_waitcnt lgkmcnt(9)
	v_mfma_f32_32x32x16_bf16 v[82:97], v[192:195], v[134:137], v[82:97]
	v_sub_f32_e32 v68, v68, v183
	v_sub_f32_e32 v80, v80, v183
	v_exp_f32_e32 v68, v68
	v_exp_f32_e32 v80, v80
	s_waitcnt lgkmcnt(8)
	v_mfma_f32_32x32x16_bf16 v[82:97], v[196:199], v[130:133], v[82:97]
	v_sub_f32_e32 v69, v69, v183
	v_sub_f32_e32 v81, v81, v183
	v_exp_f32_e32 v69, v69
	v_exp_f32_e32 v81, v81
	v_cvt_pk_bf16_f32 v194, v78, v79
	v_cvt_pk_bf16_f32 v189, v68, v69
	v_cvt_pk_bf16_f32 v195, v80, v81
	s_waitcnt lgkmcnt(7)
	v_mfma_f32_32x32x16_bf16 v[82:97], v[200:203], v[126:129], v[82:97]
	v_sub_f32_e32 v70, v70, v183
	v_exp_f32_e32 v70, v70
	s_waitcnt lgkmcnt(6)
	v_mfma_f32_32x32x16_bf16 v[82:97], v[216:219], v[122:125], v[82:97]
	v_sub_f32_e32 v71, v71, v183
	v_exp_f32_e32 v71, v71
	s_nop 0
	v_cvt_pk_bf16_f32 v190, v70, v71
	s_waitcnt lgkmcnt(5)
	v_mfma_f32_32x32x16_bf16 v[82:97], v[220:223], v[118:121], v[82:97]
	v_sub_f32_e32 v72, v72, v183
	v_exp_f32_e32 v72, v72
	s_waitcnt lgkmcnt(4)
	v_mfma_f32_32x32x16_bf16 v[82:97], v[224:227], v[114:117], v[82:97]
	v_sub_f32_e32 v73, v73, v183
	v_exp_f32_e32 v73, v73
	s_nop 0
	v_cvt_pk_bf16_f32 v191, v72, v73
	s_waitcnt lgkmcnt(3)
	v_mfma_f32_32x32x16_bf16 v[82:97], v[228:231], v[110:113], v[82:97]
	v_add_u32_e32 v204, s12, v187
	v_sub_f32_e32 v74, v74, v183
	ds_read_b128 v[196:199], v204
	ds_read_b128 v[200:203], v204 offset:32
	v_exp_f32_e32 v74, v74
	s_waitcnt lgkmcnt(4)
	v_mfma_f32_32x32x16_bf16 v[82:97], v[232:235], v[106:109], v[82:97]
	v_sub_f32_e32 v75, v75, v183
	ds_read_b128 v[216:219], v204 offset:4608
	ds_read_b128 v[220:223], v204 offset:4640
	v_exp_f32_e32 v75, v75
	s_nop 0
	v_cvt_pk_bf16_f32 v192, v74, v75
	s_waitcnt lgkmcnt(5)
	v_mfma_f32_32x32x16_bf16 v[82:97], v[236:239], v[102:105], v[82:97]
	v_sub_f32_e32 v76, v76, v183
	ds_read_b128 v[224:227], v204 offset:9216
	ds_read_b128 v[228:231], v204 offset:9248
	v_exp_f32_e32 v76, v76
	s_waitcnt lgkmcnt(6)
	v_mfma_f32_32x32x16_bf16 v[82:97], v[240:243], v[98:101], v[82:97]
	v_sub_f32_e32 v77, v77, v183
	ds_read_b128 v[232:235], v204 offset:13824
	ds_read_b128 v[236:239], v204 offset:13856
	v_exp_f32_e32 v77, v77
	s_nop 0
	v_cvt_pk_bf16_f32 v193, v76, v77
	s_and_b64 vcc, exec, s[0:1]
	s_cbranch_vccnz .LattA_slow
	s_mul_i32 s12, s36, 0x6400
	s_add_u32 s16, s80, s2
	s_addc_u32 s17, s81, s3
	s_add_u32 s16, s16, 0x30e8a000
	s_addc_u32 s17, s17, 0
	s_waitcnt lgkmcnt(0)
	v_mfma_f32_32x32x16_bf16 v[50:65], v[196:199], v[188:191], v[50:65]
	s_add_i32 m0, s12, s65
	s_nop 0
	global_load_lds_dwordx4 v208, s[16:17]
	s_add_i32 m0, s12, s66
	s_nop 0
	global_load_lds_dwordx4 v209, s[16:17]
	v_mfma_f32_32x32x16_bf16 v[34:49], v[216:219], v[188:191], v[34:49]
	s_add_i32 m0, s12, s67
	s_add_i32 s12, s12, s68
	global_load_lds_dwordx4 v210, s[16:17]
	s_add_i32 m0, s12, 0x6000
	s_nop 0
	global_load_lds_dwordx4 v211, s[16:17]
	v_mfma_f32_32x32x16_bf16 v[18:33], v[224:227], v[188:191], v[18:33]
	v_max_f32_e32 v152, v82, v83
	v_max3_f32 v152, v152, v84, v85
	s_mul_i32 s12, s36, 0x4800
	s_add_i32 s13, s12, 0xffffb800
	s_cmp_lg_u32 s36, 0
	s_cselect_b32 s13, s13, 0x9000
	s_add_i32 s13, s13, 0x12c00
	s_add_u32 s16, s82, s2
	s_addc_u32 s17, s83, s3
	s_add_u32 s16, s16, s28
	s_addc_u32 s17, s17, s29
	s_add_i32 m0, s13, s69
	s_nop 0
	global_load_lds_dwordx4 v212, s[16:17]
	v_mfma_f32_32x32x16_bf16 v[2:17], v[232:235], v[188:191], v[2:17]
	v_max3_f32 v152, v152, v86, v87
	v_max3_f32 v152, v152, v88, v89
	s_add_i32 m0, s13, s70
	s_nop 0
	global_load_lds_dwordx4 v213, s[16:17]
	s_add_i32 m0, s13, s71
	s_nop 0
	global_load_lds_dwordx4 v214, s[16:17]
	v_mfma_f32_32x32x16_bf16 v[50:65], v[200:203], v[192:195], v[50:65]
	v_max3_f32 v152, v152, v90, v91
	v_max3_f32 v152, v152, v92, v93
	v_mfma_f32_32x32x16_bf16 v[34:49], v[220:223], v[192:195], v[34:49]
	v_max3_f32 v152, v152, v94, v95
	v_max3_f32 v152, v152, v96, v97
	v_mfma_f32_32x32x16_bf16 v[18:33], v[228:231], v[192:195], v[18:33]
	v_mfma_f32_32x32x16_bf16 v[2:17], v[236:239], v[192:195], v[2:17]
	v_mov_b32_e32 v153, v152
	s_nop 1
	v_permlane32_swap_b32_e32 v153, v152
	v_max_f32_e32 v152, v152, v153
	s_branch .LattA_join
